# v131 + SwiGLU (FFN-in) epilogue: SGPR base + one 32-bit VGPR offset for the 8 stores, the 21 per-block address VALU ops (7 v_mad_i64_i32) removed
# baseline (speedup 1.0000x reference)
; __device__ __forceinline__ unsigned cvt_pk_bf16(float lo, float hi) { unsigned r; asm volatile("v_cvt_pk_bf16_f32 %0, %1, %2" : "=v"(r) : "v"(lo), "v"(hi)); return r; }
;     __device__ __forceinline__ void operator()(const f32x4 (&acc)[2][2][4][2], const Unit& u, int wr, int wc, int fr, int fq) const {
;         const int row0 = u.pm * BM + wr * 64 + fr, col0 = u.pn * HALF + wc * 32 + 8 * fq;
; #pragma unroll
;         for (int ai = 0; ai < 2; ++ai)
; #pragma unroll
;             for (int m = 0; m < 4; ++m) { bf16_t* rowp = O + (size_t)(row0 + ai * HALF + m * 16) * ldc + col0;
;                 const f32x4 g0 = acc[ai][0][m][0], g1 = acc[ai][0][m][1], u0 = acc[ai][1][m][0], u1 = acc[ai][1][m][1];
;                 f32x4 e0 = g0 * -1.4426950408889634f, e1 = g1 * -1.4426950408889634f;
;                 const f32x4 p0 = g0 * u0, p1 = g1 * u1;
;                 __builtin_amdgcn_sched_barrier(0);
; #pragma unroll
;                 for (int i = 0; i < 4; ++i) { e0[i] = __builtin_amdgcn_exp2f(e0[i]); e1[i] = __builtin_amdgcn_exp2f(e1[i]); }
;                 __builtin_amdgcn_sched_barrier(0);
;                 e0 = e0 + 1.0f; e1 = e1 + 1.0f;
;                 __builtin_amdgcn_sched_barrier(0);
; #pragma unroll
;                 for (int i = 0; i < 4; ++i) { e0[i] = __builtin_amdgcn_rcpf(e0[i]); e1[i] = __builtin_amdgcn_rcpf(e1[i]); }
;                 __builtin_amdgcn_sched_barrier(0);
;                 const f32x4 o0 = p0 * e0, o1 = p1 * e1;
;                 u32x4 w; w.x = cvt_pk_bf16(o0[0], o0[1]); w.y = cvt_pk_bf16(o0[2], o0[3]); w.z = cvt_pk_bf16(o1[0], o1[1]); w.w = cvt_pk_bf16(o1[2], o1[3]);
;                 *(u32x4*)rowp = w; }
.LBB0_310:
	v_lshl_add_u32 v139, s35, 8, v135
	v_lshl_or_b32 v140, s34, 7, v136
	v_mov_b64_e32 v[130:131], s[4:5]
	s_movk_i32 s34, 0x2c00
	v_mul_u32_u24_e32 v164, s34, v139
	s_mov_b32 s36, 0xbfb8aa3b
	v_ashrrev_i32_e32 v141, 31, v140
	v_pk_mul_f32 v[146:147], v[128:129], s[36:37] op_sel_hi:[1,0]
	v_pk_mul_f32 v[148:149], v[126:127], s[36:37] op_sel_hi:[1,0]
	v_pk_mul_f32 v[150:151], v[120:121], s[36:37] op_sel_hi:[1,0]
	v_pk_mul_f32 v[152:153], v[118:119], s[36:37] op_sel_hi:[1,0]
	v_pk_mul_f32 v[124:125], v[128:129], v[124:125]
	v_pk_mul_f32 v[126:127], v[126:127], v[122:123]
	v_lshlrev_b64 v[122:123], 1, v[140:141]
	v_exp_f32_e32 v128, v148
	v_exp_f32_e32 v148, v152
	v_exp_f32_e32 v129, v149
	v_exp_f32_e32 v149, v153
	v_exp_f32_e32 v146, v146
	v_exp_f32_e32 v150, v150
	v_exp_f32_e32 v147, v147
	v_exp_f32_e32 v151, v151
	v_add_u32_e32 v164, v164, v122
	v_pk_add_f32 v[144:145], v[146:147], 1.0 op_sel_hi:[1,0]
	v_pk_add_f32 v[128:129], v[128:129], 1.0 op_sel_hi:[1,0]
	v_pk_add_f32 v[146:147], v[150:151], 1.0 op_sel_hi:[1,0]
	v_pk_add_f32 v[148:149], v[148:149], 1.0 op_sel_hi:[1,0]
	v_rcp_f32_e32 v128, v128
	v_rcp_f32_e32 v148, v148
	v_rcp_f32_e32 v129, v129
	v_rcp_f32_e32 v149, v149
	v_rcp_f32_e32 v144, v144
	v_rcp_f32_e32 v146, v146
	v_rcp_f32_e32 v145, v145
	v_rcp_f32_e32 v147, v147
	v_pk_mul_f32 v[116:117], v[120:121], v[116:117]
	v_pk_mul_f32 v[114:115], v[118:119], v[114:115]
	v_pk_mul_f32 v[118:119], v[144:145], v[124:125]
	v_pk_mul_f32 v[120:121], v[128:129], v[126:127]
	v_pk_mul_f32 v[124:125], v[146:147], v[116:117]
	v_pk_mul_f32 v[116:117], v[148:149], v[114:115]
	v_cvt_pk_bf16_f32 v114, v120, v121
	v_cvt_pk_bf16_f32 v115, v118, v119
	v_pk_mul_f32 v[118:119], v[110:111], s[36:37] op_sel_hi:[1,0]
	v_cvt_pk_bf16_f32 v116, v116, v117
	v_cvt_pk_bf16_f32 v117, v124, v125
	global_store_dwordx4 v164, v[114:117], s[4:5]
	v_add_u32_e32 v164, 0x2c000, v164
	v_pk_mul_f32 v[120:121], v[104:105], s[36:37] op_sel_hi:[1,0]
	v_pk_mul_f32 v[124:125], v[102:103], s[36:37] op_sel_hi:[1,0]
	v_pk_mul_f32 v[116:117], v[112:113], s[36:37] op_sel_hi:[1,0]
	v_pk_mul_f32 v[108:109], v[112:113], v[108:109]
	v_pk_mul_f32 v[106:107], v[110:111], v[106:107]
	v_exp_f32_e32 v110, v118
	v_exp_f32_e32 v112, v124
	v_exp_f32_e32 v111, v119
	v_exp_f32_e32 v113, v125
	v_exp_f32_e32 v116, v116
	v_exp_f32_e32 v118, v120
	v_exp_f32_e32 v117, v117
	v_exp_f32_e32 v119, v121
	v_pk_add_f32 v[116:117], v[116:117], 1.0 op_sel_hi:[1,0]
	v_pk_add_f32 v[110:111], v[110:111], 1.0 op_sel_hi:[1,0]
	v_pk_add_f32 v[118:119], v[118:119], 1.0 op_sel_hi:[1,0]
	v_pk_add_f32 v[112:113], v[112:113], 1.0 op_sel_hi:[1,0]
	v_rcp_f32_e32 v110, v110
	v_rcp_f32_e32 v112, v112
	v_rcp_f32_e32 v111, v111
	v_rcp_f32_e32 v113, v113
	v_rcp_f32_e32 v116, v116
	v_rcp_f32_e32 v118, v118
	v_rcp_f32_e32 v117, v117
	v_rcp_f32_e32 v119, v119
	v_pk_mul_f32 v[100:101], v[104:105], v[100:101]
	v_pk_mul_f32 v[98:99], v[102:103], v[98:99]
	v_pk_mul_f32 v[104:105], v[110:111], v[106:107]
	v_pk_mul_f32 v[106:107], v[118:119], v[100:101]
	v_pk_mul_f32 v[100:101], v[112:113], v[98:99]
	v_cvt_pk_bf16_f32 v98, v104, v105
	v_pk_mul_f32 v[102:103], v[116:117], v[108:109]
	v_pk_mul_f32 v[104:105], v[88:89], s[36:37] op_sel_hi:[1,0]
	v_cvt_pk_bf16_f32 v99, v102, v103
	v_cvt_pk_bf16_f32 v100, v100, v101
	v_cvt_pk_bf16_f32 v101, v106, v107
	global_store_dwordx4 v164, v[98:101], s[4:5]
	v_add_u32_e32 v164, 0x2c000, v164
	v_pk_mul_f32 v[102:103], v[94:95], s[36:37] op_sel_hi:[1,0]
	v_pk_mul_f32 v[106:107], v[86:87], s[36:37] op_sel_hi:[1,0]
	v_pk_mul_f32 v[100:101], v[96:97], s[36:37] op_sel_hi:[1,0]
	v_pk_mul_f32 v[92:93], v[96:97], v[92:93]
	v_pk_mul_f32 v[90:91], v[94:95], v[90:91]
	v_exp_f32_e32 v94, v102
	v_exp_f32_e32 v96, v106
	v_exp_f32_e32 v95, v103
	v_exp_f32_e32 v97, v107
	v_exp_f32_e32 v100, v100
	v_exp_f32_e32 v102, v104
	v_exp_f32_e32 v101, v101
	v_exp_f32_e32 v103, v105
	v_pk_add_f32 v[100:101], v[100:101], 1.0 op_sel_hi:[1,0]
	v_pk_add_f32 v[94:95], v[94:95], 1.0 op_sel_hi:[1,0]
	v_pk_add_f32 v[102:103], v[102:103], 1.0 op_sel_hi:[1,0]
	v_pk_add_f32 v[96:97], v[96:97], 1.0 op_sel_hi:[1,0]
	v_rcp_f32_e32 v94, v94
	v_rcp_f32_e32 v96, v96
	v_rcp_f32_e32 v95, v95
	v_rcp_f32_e32 v97, v97
	v_rcp_f32_e32 v100, v100
	v_rcp_f32_e32 v102, v102
	v_rcp_f32_e32 v101, v101
	v_rcp_f32_e32 v103, v103
	v_pk_mul_f32 v[84:85], v[88:89], v[84:85]
	v_pk_mul_f32 v[82:83], v[86:87], v[82:83]
	v_pk_mul_f32 v[88:89], v[94:95], v[90:91]
	v_pk_mul_f32 v[90:91], v[102:103], v[84:85]
	v_pk_mul_f32 v[84:85], v[96:97], v[82:83]
	v_cvt_pk_bf16_f32 v82, v88, v89
	v_pk_mul_f32 v[86:87], v[100:101], v[92:93]
	v_pk_mul_f32 v[88:89], v[72:73], s[36:37] op_sel_hi:[1,0]
	v_cvt_pk_bf16_f32 v83, v86, v87
	v_cvt_pk_bf16_f32 v84, v84, v85
	v_cvt_pk_bf16_f32 v85, v90, v91
	global_store_dwordx4 v164, v[82:85], s[4:5]
	v_add_u32_e32 v164, 0x2c000, v164
	v_pk_mul_f32 v[86:87], v[78:79], s[36:37] op_sel_hi:[1,0]
	v_pk_mul_f32 v[90:91], v[70:71], s[36:37] op_sel_hi:[1,0]
	v_pk_mul_f32 v[84:85], v[80:81], s[36:37] op_sel_hi:[1,0]
	v_pk_mul_f32 v[76:77], v[80:81], v[76:77]
	v_pk_mul_f32 v[74:75], v[78:79], v[74:75]
	v_exp_f32_e32 v78, v86
	v_exp_f32_e32 v80, v90
	v_exp_f32_e32 v79, v87
	v_exp_f32_e32 v81, v91
	v_exp_f32_e32 v84, v84
	v_exp_f32_e32 v86, v88
	v_exp_f32_e32 v85, v85
	v_exp_f32_e32 v87, v89
	v_pk_add_f32 v[84:85], v[84:85], 1.0 op_sel_hi:[1,0]
	v_pk_add_f32 v[78:79], v[78:79], 1.0 op_sel_hi:[1,0]
	v_pk_add_f32 v[86:87], v[86:87], 1.0 op_sel_hi:[1,0]
	v_pk_add_f32 v[80:81], v[80:81], 1.0 op_sel_hi:[1,0]
	v_rcp_f32_e32 v78, v78
	v_rcp_f32_e32 v80, v80
	v_rcp_f32_e32 v79, v79
	v_rcp_f32_e32 v81, v81
	v_rcp_f32_e32 v84, v84
	v_rcp_f32_e32 v86, v86
; __device__ __forceinline__ unsigned cvt_pk_bf16(float lo, float hi) { unsigned r; asm volatile("v_cvt_pk_bf16_f32 %0, %1, %2" : "=v"(r) : "v"(lo), "v"(hi)); return r; }
; #define PG8_BAR __builtin_amdgcn_s_barrier()
;     __device__ __forceinline__ void operator()(const f32x4 (&acc)[2][2][4][2], const Unit& u, int wr, int wc, int fr, int fq) const {
;     ...
;             for (int m = 0; m < 4; ++m) { bf16_t* rowp = O + (size_t)(row0 + ai * HALF + m * 16) * ldc + col0;
;                 const f32x4 g0 = acc[ai][0][m][0], g1 = acc[ai][0][m][1], u0 = acc[ai][1][m][0], u1 = acc[ai][1][m][1];
;                 f32x4 e0 = g0 * -1.4426950408889634f, e1 = g1 * -1.4426950408889634f;
;                 const f32x4 p0 = g0 * u0, p1 = g1 * u1;
;                 __builtin_amdgcn_sched_barrier(0);
; #pragma unroll
;                 for (int i = 0; i < 4; ++i) { e0[i] = __builtin_amdgcn_exp2f(e0[i]); e1[i] = __builtin_amdgcn_exp2f(e1[i]); }
;                 __builtin_amdgcn_sched_barrier(0);
;                 e0 = e0 + 1.0f; e1 = e1 + 1.0f;
;                 __builtin_amdgcn_sched_barrier(0);
; #pragma unroll
;                 for (int i = 0; i < 4; ++i) { e0[i] = __builtin_amdgcn_rcpf(e0[i]); e1[i] = __builtin_amdgcn_rcpf(e1[i]); }
;                 __builtin_amdgcn_sched_barrier(0);
;                 const f32x4 o0 = p0 * e0, o1 = p1 * e1;
;                 u32x4 w; w.x = cvt_pk_bf16(o0[0], o0[1]); w.y = cvt_pk_bf16(o0[2], o0[3]); w.z = cvt_pk_bf16(o1[0], o1[1]); w.w = cvt_pk_bf16(o1[2], o1[3]);
;                 *(u32x4*)rowp = w; }
; template <class Epi, class Sched, bool ALIGN_EPI = false>
; __device__ __forceinline__ void gemm_phase(PG8_LAS unsigned char* lds, const Gemm g, const Sched& S, const Epi& E, const int tid) {
;     ...
;         if (!has_next) break;
; #pragma unroll
;         for (int a = 0; a < 2; ++a)
; #pragma unroll
;             for (int b = 0; b < 2; ++b)
; #pragma unroll
;                 for (int m = 0; m < 4; ++m)
; #pragma unroll
;                     for (int n = 0; n < 2; ++n) acc[a][b][m][n] = (f32x4){0.f, 0.f, 0.f, 0.f};
;         cur = nxt; cA = nA; cB = nB; ++ui;
;         if constexpr (ALIGN_EPI) { if (wr == 1) PG8_BAR; }
	v_rcp_f32_e32 v85, v85
	v_rcp_f32_e32 v87, v87
	v_pk_mul_f32 v[68:69], v[72:73], v[68:69]
	v_pk_mul_f32 v[66:67], v[70:71], v[66:67]
	v_pk_mul_f32 v[72:73], v[78:79], v[74:75]
	v_pk_mul_f32 v[74:75], v[86:87], v[68:69]
	v_pk_mul_f32 v[68:69], v[80:81], v[66:67]
	v_cvt_pk_bf16_f32 v66, v72, v73
	v_pk_mul_f32 v[70:71], v[84:85], v[76:77]
	v_pk_mul_f32 v[72:73], v[56:57], s[36:37] op_sel_hi:[1,0]
	v_cvt_pk_bf16_f32 v67, v70, v71
	v_cvt_pk_bf16_f32 v68, v68, v69
	v_cvt_pk_bf16_f32 v69, v74, v75
	global_store_dwordx4 v164, v[66:69], s[4:5]
	v_add_u32_e32 v164, 0xdc000, v164
	v_pk_mul_f32 v[70:71], v[62:63], s[36:37] op_sel_hi:[1,0]
	v_pk_mul_f32 v[74:75], v[54:55], s[36:37] op_sel_hi:[1,0]
	v_pk_mul_f32 v[68:69], v[64:65], s[36:37] op_sel_hi:[1,0]
	v_pk_mul_f32 v[60:61], v[64:65], v[60:61]
	v_pk_mul_f32 v[58:59], v[62:63], v[58:59]
	v_exp_f32_e32 v62, v70
	v_exp_f32_e32 v64, v74
	v_exp_f32_e32 v63, v71
	v_exp_f32_e32 v65, v75
	v_exp_f32_e32 v68, v68
	v_exp_f32_e32 v70, v72
	v_exp_f32_e32 v69, v69
	v_exp_f32_e32 v71, v73
	v_pk_add_f32 v[68:69], v[68:69], 1.0 op_sel_hi:[1,0]
	v_pk_add_f32 v[62:63], v[62:63], 1.0 op_sel_hi:[1,0]
	v_pk_add_f32 v[70:71], v[70:71], 1.0 op_sel_hi:[1,0]
	v_pk_add_f32 v[64:65], v[64:65], 1.0 op_sel_hi:[1,0]
	v_rcp_f32_e32 v62, v62
	v_rcp_f32_e32 v64, v64
	v_rcp_f32_e32 v63, v63
	v_rcp_f32_e32 v65, v65
	v_rcp_f32_e32 v68, v68
	v_rcp_f32_e32 v70, v70
	v_rcp_f32_e32 v69, v69
	v_rcp_f32_e32 v71, v71
	v_pk_mul_f32 v[52:53], v[56:57], v[52:53]
	v_pk_mul_f32 v[50:51], v[54:55], v[50:51]
	v_pk_mul_f32 v[56:57], v[62:63], v[58:59]
	v_pk_mul_f32 v[58:59], v[70:71], v[52:53]
	v_pk_mul_f32 v[52:53], v[64:65], v[50:51]
	v_cvt_pk_bf16_f32 v50, v56, v57
	v_pk_mul_f32 v[54:55], v[68:69], v[60:61]
	v_pk_mul_f32 v[56:57], v[40:41], s[36:37] op_sel_hi:[1,0]
	v_cvt_pk_bf16_f32 v51, v54, v55
	v_cvt_pk_bf16_f32 v52, v52, v53
	v_cvt_pk_bf16_f32 v53, v58, v59
	global_store_dwordx4 v164, v[50:53], s[4:5]
	v_add_u32_e32 v164, 0x2c000, v164
	v_pk_mul_f32 v[54:55], v[46:47], s[36:37] op_sel_hi:[1,0]
	v_pk_mul_f32 v[58:59], v[38:39], s[36:37] op_sel_hi:[1,0]
	v_pk_mul_f32 v[52:53], v[48:49], s[36:37] op_sel_hi:[1,0]
	v_pk_mul_f32 v[44:45], v[48:49], v[44:45]
	v_pk_mul_f32 v[42:43], v[46:47], v[42:43]
	v_exp_f32_e32 v46, v54
	v_exp_f32_e32 v48, v58
	v_exp_f32_e32 v47, v55
	v_exp_f32_e32 v49, v59
	v_exp_f32_e32 v52, v52
	v_exp_f32_e32 v54, v56
	v_exp_f32_e32 v53, v53
	v_exp_f32_e32 v55, v57
	v_pk_add_f32 v[52:53], v[52:53], 1.0 op_sel_hi:[1,0]
	v_pk_add_f32 v[46:47], v[46:47], 1.0 op_sel_hi:[1,0]
	v_pk_add_f32 v[54:55], v[54:55], 1.0 op_sel_hi:[1,0]
	v_pk_add_f32 v[48:49], v[48:49], 1.0 op_sel_hi:[1,0]
	v_rcp_f32_e32 v46, v46
	v_rcp_f32_e32 v48, v48
	v_rcp_f32_e32 v47, v47
	v_rcp_f32_e32 v49, v49
	v_rcp_f32_e32 v52, v52
	v_rcp_f32_e32 v54, v54
	v_rcp_f32_e32 v53, v53
	v_rcp_f32_e32 v55, v55
	v_pk_mul_f32 v[36:37], v[40:41], v[36:37]
	v_pk_mul_f32 v[34:35], v[38:39], v[34:35]
	v_pk_mul_f32 v[40:41], v[46:47], v[42:43]
	v_pk_mul_f32 v[42:43], v[54:55], v[36:37]
	v_pk_mul_f32 v[36:37], v[48:49], v[34:35]
	v_cvt_pk_bf16_f32 v34, v40, v41
	v_pk_mul_f32 v[38:39], v[52:53], v[44:45]
	v_pk_mul_f32 v[40:41], v[24:25], s[36:37] op_sel_hi:[1,0]
	v_cvt_pk_bf16_f32 v35, v38, v39
	v_cvt_pk_bf16_f32 v36, v36, v37
	v_cvt_pk_bf16_f32 v37, v42, v43
	global_store_dwordx4 v164, v[34:37], s[4:5]
	v_add_u32_e32 v164, 0x2c000, v164
	v_pk_mul_f32 v[38:39], v[30:31], s[36:37] op_sel_hi:[1,0]
	v_pk_mul_f32 v[42:43], v[22:23], s[36:37] op_sel_hi:[1,0]
	v_pk_mul_f32 v[36:37], v[32:33], s[36:37] op_sel_hi:[1,0]
	v_pk_mul_f32 v[28:29], v[32:33], v[28:29]
	v_pk_mul_f32 v[26:27], v[30:31], v[26:27]
	v_exp_f32_e32 v30, v38
	v_exp_f32_e32 v32, v42
	v_exp_f32_e32 v31, v39
	v_exp_f32_e32 v33, v43
	v_exp_f32_e32 v36, v36
	v_exp_f32_e32 v38, v40
	v_exp_f32_e32 v37, v37
	v_exp_f32_e32 v39, v41
	v_pk_add_f32 v[36:37], v[36:37], 1.0 op_sel_hi:[1,0]
	v_pk_add_f32 v[30:31], v[30:31], 1.0 op_sel_hi:[1,0]
	v_pk_add_f32 v[38:39], v[38:39], 1.0 op_sel_hi:[1,0]
	v_pk_add_f32 v[32:33], v[32:33], 1.0 op_sel_hi:[1,0]
	v_rcp_f32_e32 v30, v30
	v_rcp_f32_e32 v32, v32
	v_rcp_f32_e32 v31, v31
	v_rcp_f32_e32 v33, v33
	v_rcp_f32_e32 v36, v36
	v_rcp_f32_e32 v38, v38
	v_rcp_f32_e32 v37, v37
	v_rcp_f32_e32 v39, v39
	v_pk_mul_f32 v[20:21], v[24:25], v[20:21]
	v_pk_mul_f32 v[18:19], v[22:23], v[18:19]
	v_pk_mul_f32 v[24:25], v[30:31], v[26:27]
	v_pk_mul_f32 v[26:27], v[38:39], v[20:21]
	v_pk_mul_f32 v[20:21], v[32:33], v[18:19]
	v_cvt_pk_bf16_f32 v18, v24, v25
	v_pk_mul_f32 v[22:23], v[36:37], v[28:29]
	v_pk_mul_f32 v[24:25], v[8:9], s[36:37] op_sel_hi:[1,0]
	v_cvt_pk_bf16_f32 v19, v22, v23
	v_cvt_pk_bf16_f32 v20, v20, v21
	v_cvt_pk_bf16_f32 v21, v26, v27
	global_store_dwordx4 v164, v[18:21], s[4:5]
	v_add_u32_e32 v164, 0x2c000, v164
	v_pk_mul_f32 v[22:23], v[14:15], s[36:37] op_sel_hi:[1,0]
	v_pk_mul_f32 v[26:27], v[6:7], s[36:37] op_sel_hi:[1,0]
	v_pk_mul_f32 v[20:21], v[16:17], s[36:37] op_sel_hi:[1,0]
	v_pk_mul_f32 v[12:13], v[16:17], v[12:13]
	v_pk_mul_f32 v[10:11], v[14:15], v[10:11]
	v_exp_f32_e32 v14, v22
	v_exp_f32_e32 v16, v26
	v_exp_f32_e32 v15, v23
	v_exp_f32_e32 v17, v27
	v_exp_f32_e32 v20, v20
	v_exp_f32_e32 v22, v24
	v_exp_f32_e32 v21, v21
	v_exp_f32_e32 v23, v25
	v_pk_add_f32 v[20:21], v[20:21], 1.0 op_sel_hi:[1,0]
	v_pk_add_f32 v[14:15], v[14:15], 1.0 op_sel_hi:[1,0]
	v_pk_add_f32 v[22:23], v[22:23], 1.0 op_sel_hi:[1,0]
	v_pk_add_f32 v[16:17], v[16:17], 1.0 op_sel_hi:[1,0]
	v_rcp_f32_e32 v14, v14
	v_rcp_f32_e32 v16, v16
	v_rcp_f32_e32 v15, v15
	v_rcp_f32_e32 v17, v17
	v_rcp_f32_e32 v20, v20
	v_rcp_f32_e32 v22, v22
	v_rcp_f32_e32 v21, v21
	v_rcp_f32_e32 v23, v23
	v_pk_mul_f32 v[4:5], v[8:9], v[4:5]
	v_pk_mul_f32 v[2:3], v[6:7], v[2:3]
	v_pk_mul_f32 v[8:9], v[14:15], v[10:11]
	v_pk_mul_f32 v[10:11], v[22:23], v[4:5]
	v_pk_mul_f32 v[4:5], v[16:17], v[2:3]
	s_and_b64 vcc, exec, s[40:41]
	s_mov_b64 s[18:19], -1
	s_movk_i32 s38, 0x800
	s_movk_i32 s39, 0x200
	v_pk_mul_f32 v[6:7], v[20:21], v[12:13]
	v_cvt_pk_bf16_f32 v2, v8, v9
	s_nop 0
	v_cvt_pk_bf16_f32 v3, v6, v7
	v_cvt_pk_bf16_f32 v4, v4, v5
	v_cvt_pk_bf16_f32 v5, v10, v11
	global_store_dwordx4 v164, v[2:5], s[4:5]
	s_cbranch_vccnz .LBB0_301
	s_andn2_b64 vcc, exec, s[0:1]
	s_cbranch_vccnz .LBB0_300
	s_barrier
	s_branch .LBB0_300
